# baseline (speedup 1.0000x reference)
.LBB1_46:
	s_or_b64 exec, exec, s[0:1]
	v_lshrrev_b32_e32 v1, 3, v25
	v_lshrrev_b32_e32 v57, 6, v0
	v_lshlrev_b32_e32 v58, 2, v1
	s_waitcnt lgkmcnt(0)
	s_barrier
	v_lshlrev_b32_e32 v0, 4, v0
	v_lshl_or_b32 v59, v57, 5, v58
	s_bfe_u32 s0, s2, 0x20001
	v_and_b32_e32 v56, 0x70, v0
	ds_read_b32 v0, v59 offset:11344
	v_xor_b32_e32 v63, 3, v57
	v_lshl_or_b32 v63, v63, 5, v58
	ds_read_b32 v70, v63 offset:11472
	ds_read_b32 v71, v59 offset:11600
	ds_read_b32 v63, v63 offset:11728
	s_mul_i32 s1, s0, 0x61a800
	s_add_u32 s14, s14, s1
	s_addc_u32 s15, s15, 0
	s_and_b32 s21, s19, 0xffff
	s_lshl_b32 s34, s3, 7
	s_waitcnt lgkmcnt(0)
	s_movk_i32 s35, 0x2840
	v_lshl_add_u32 v64, v70, 2, s35
	v_lshl_add_u32 v66, v71, 2, s35
	v_lshl_add_u32 v68, v63, 2, s35
	ds_read2_b32 v[64:65], v64 offset1:1
	ds_read2_b32 v[66:67], v66 offset1:1
	ds_read2_b32 v[68:69], v68 offset1:1
	s_cmp_gt_i32 s33, 0
	v_add_f32_e64 v40, s63, 1.0
	s_cselect_b64 s[16:17], -1, 0
	s_lshl_b32 s19, s0, 7
	v_add_u32_e32 v60, s34, v0
	s_mov_b32 s0, 0xc350
	s_mov_b32 s23, 0x20000
	s_mov_b32 s22, 0x186a000
	v_mov_b32_e32 v41, v40
	v_cmp_gt_i32_e32 vcc, s0, v60
	s_and_saveexec_b64 s[24:25], vcc
	s_cbranch_execz .LBB1_81
	v_lshl_or_b32 v1, v60, 7, v56
	global_load_dwordx4 v[4:7], v1, s[14:15]
	v_mov_b32_e32 v1, 0x2840
	v_lshl_add_u32 v0, v0, 2, v1
	ds_read2_b32 v[46:47], v0 offset1:1
	v_mov_b32_e32 v0, 0
	v_mov_b32_e32 v1, v0
	v_mov_b64_e32 v[44:45], v[0:1]
	v_mov_b64_e32 v[42:43], v[0:1]
	s_waitcnt lgkmcnt(0)
	v_cmp_lt_i32_e32 vcc, v46, v47
	s_waitcnt vmcnt(1)
	v_mov_b64_e32 v[2:3], v[0:1]
	s_and_saveexec_b64 s[26:27], vcc
	s_cbranch_execz .LBB1_75
	v_mov_b32_e32 v2, v0
	v_mov_b32_e32 v3, v0
	v_mov_b32_e32 v1, v0
	v_mov_b64_e32 v[10:11], v[2:3]
	v_mov_b64_e32 v[14:15], v[2:3]
	v_mov_b64_e32 v[18:19], v[2:3]
	v_mov_b64_e32 v[22:23], v[2:3]
	v_mov_b64_e32 v[26:27], v[2:3]
	v_mov_b64_e32 v[30:31], v[2:3]
	v_mov_b64_e32 v[34:35], v[2:3]
	v_lshlrev_b32_e32 v61, 2, v46
	v_add_u32_e32 v46, 7, v46
	s_mov_b64 s[28:29], 0
	s_mov_b32 s20, 0x7fff80
	v_mov_b64_e32 v[8:9], v[0:1]
	v_mov_b64_e32 v[12:13], v[0:1]
	v_mov_b64_e32 v[16:17], v[0:1]
	v_mov_b64_e32 v[20:21], v[0:1]
	v_mov_b64_e32 v[24:25], v[0:1]
	v_mov_b64_e32 v[28:29], v[0:1]
	v_mov_b64_e32 v[32:33], v[0:1]
	v_mov_b32_e32 v42, v0
	v_mov_b32_e32 v43, v0
	v_mov_b32_e32 v44, v0
	v_mov_b32_e32 v45, v0
	s_branch .LBB1_50

.LBB1_81:
	s_or_b64 exec, exec, s[24:25]
	v_xor_b32_e32 v0, 3, v57
	v_lshl_or_b32 v57, v0, 5, v58
	s_waitcnt vmcnt(1)
	v_mov_b32_e32 v4, v70
	s_mov_b32 s0, 0xc350
	v_add_u32_e32 v59, 0x2c50, v59
	s_waitcnt lgkmcnt(0)
	v_add_u32_e32 v58, s34, v4
	v_cmp_gt_i32_e32 vcc, s0, v58
	s_and_saveexec_b64 s[24:25], vcc
	s_cbranch_execz .LBB1_106
	v_lshl_or_b32 v0, v58, 7, v56
	global_load_dwordx4 v[0:3], v0, s[14:15]
	v_mov_b32_e32 v46, v64
	v_mov_b32_e32 v47, v65
	v_mov_b32_e32 v4, 0
	v_mov_b32_e32 v5, v4
	v_mov_b64_e32 v[44:45], v[4:5]
	v_mov_b64_e32 v[42:43], v[4:5]
	s_waitcnt lgkmcnt(0)
	v_cmp_lt_i32_e32 vcc, v46, v47
	v_mov_b64_e32 v[6:7], v[4:5]
	s_and_saveexec_b64 s[26:27], vcc
	s_cbranch_execz .LBB1_100
	v_mov_b32_e32 v6, v4
	v_mov_b32_e32 v7, v4
	v_mov_b32_e32 v5, v4
	v_mov_b64_e32 v[10:11], v[6:7]
	v_mov_b64_e32 v[14:15], v[6:7]
	v_mov_b64_e32 v[18:19], v[6:7]
	v_mov_b64_e32 v[22:23], v[6:7]
	v_mov_b64_e32 v[26:27], v[6:7]
	v_mov_b64_e32 v[30:31], v[6:7]
	v_mov_b64_e32 v[34:35], v[6:7]
	v_lshlrev_b32_e32 v60, 2, v46
	s_mov_b64 s[28:29], 0
	s_mov_b32 s20, 0x7fff80
	v_mov_b64_e32 v[8:9], v[4:5]
	v_mov_b64_e32 v[12:13], v[4:5]
	v_mov_b64_e32 v[16:17], v[4:5]
	v_mov_b64_e32 v[20:21], v[4:5]
	v_mov_b64_e32 v[24:25], v[4:5]
	v_mov_b64_e32 v[28:29], v[4:5]
	v_mov_b64_e32 v[32:33], v[4:5]
	v_mov_b32_e32 v42, v4
	v_mov_b32_e32 v43, v4
	v_mov_b32_e32 v44, v4
	v_mov_b32_e32 v45, v4
	s_branch .LBB1_85

.LBB1_106:
	s_or_b64 exec, exec, s[24:25]
	v_mov_b32_e32 v4, v71
	s_mov_b32 s0, 0xc350
	v_add_u32_e32 v57, 0x2c50, v57
	s_waitcnt lgkmcnt(0)
	v_add_u32_e32 v58, s34, v4
	v_cmp_gt_i32_e32 vcc, s0, v58
	s_and_saveexec_b64 s[24:25], vcc
	s_cbranch_execz .LBB1_131
	v_lshl_or_b32 v0, v58, 7, v56
	global_load_dwordx4 v[0:3], v0, s[14:15]
	v_mov_b32_e32 v46, v66
	v_mov_b32_e32 v47, v67
	v_mov_b32_e32 v4, 0
	v_mov_b32_e32 v5, v4
	v_mov_b64_e32 v[44:45], v[4:5]
	v_mov_b64_e32 v[42:43], v[4:5]
	s_waitcnt lgkmcnt(0)
	v_cmp_lt_i32_e32 vcc, v46, v47
	v_mov_b64_e32 v[6:7], v[4:5]
	s_and_saveexec_b64 s[26:27], vcc
	s_cbranch_execz .LBB1_125
	v_mov_b32_e32 v6, v4
	v_mov_b32_e32 v7, v4
	v_mov_b32_e32 v5, v4
	v_mov_b64_e32 v[10:11], v[6:7]
	v_mov_b64_e32 v[14:15], v[6:7]
	v_mov_b64_e32 v[18:19], v[6:7]
	v_mov_b64_e32 v[22:23], v[6:7]
	v_mov_b64_e32 v[26:27], v[6:7]
	v_mov_b64_e32 v[30:31], v[6:7]
	v_mov_b64_e32 v[34:35], v[6:7]
	v_lshlrev_b32_e32 v59, 2, v46
	s_mov_b64 s[28:29], 0
	s_mov_b32 s20, 0x7fff80
	v_mov_b64_e32 v[8:9], v[4:5]
	v_mov_b64_e32 v[12:13], v[4:5]
	v_mov_b64_e32 v[16:17], v[4:5]
	v_mov_b64_e32 v[20:21], v[4:5]
	v_mov_b64_e32 v[24:25], v[4:5]
	v_mov_b64_e32 v[28:29], v[4:5]
	v_mov_b64_e32 v[32:33], v[4:5]
	v_mov_b32_e32 v42, v4
	v_mov_b32_e32 v43, v4
	v_mov_b32_e32 v44, v4
	v_mov_b32_e32 v45, v4
	s_branch .LBB1_110

.LBB1_131:
	s_or_b64 exec, exec, s[24:25]
	v_mov_b32_e32 v4, v63
	s_mov_b32 s0, 0xc350
	s_waitcnt lgkmcnt(0)
	v_add_u32_e32 v57, s34, v4
	v_cmp_gt_i32_e32 vcc, s0, v57
	s_and_saveexec_b64 s[0:1], vcc
	s_cbranch_execz .LBB1_156
	v_lshl_or_b32 v0, v57, 7, v56
	global_load_dwordx4 v[0:3], v0, s[14:15]
	v_mov_b32_e32 v46, v68
	v_mov_b32_e32 v47, v69
	v_mov_b32_e32 v4, 0
	v_mov_b32_e32 v5, v4
	v_mov_b64_e32 v[44:45], v[4:5]
	v_mov_b64_e32 v[42:43], v[4:5]
	s_waitcnt lgkmcnt(0)
	v_cmp_lt_i32_e32 vcc, v46, v47
	v_mov_b64_e32 v[6:7], v[4:5]
	s_and_saveexec_b64 s[24:25], vcc
	s_cbranch_execz .LBB1_150
	v_mov_b32_e32 v6, v4
	v_mov_b32_e32 v7, v4
	v_mov_b32_e32 v5, v4
	v_mov_b64_e32 v[10:11], v[6:7]
	v_mov_b64_e32 v[14:15], v[6:7]
	v_mov_b64_e32 v[18:19], v[6:7]
	v_mov_b64_e32 v[22:23], v[6:7]
	v_mov_b64_e32 v[26:27], v[6:7]
	v_mov_b64_e32 v[30:31], v[6:7]
	v_mov_b64_e32 v[34:35], v[6:7]
	v_lshlrev_b32_e32 v58, 2, v46
	s_mov_b64 s[26:27], 0
	s_mov_b32 s20, 0x7fff80
	v_mov_b64_e32 v[8:9], v[4:5]
	v_mov_b64_e32 v[12:13], v[4:5]
	v_mov_b64_e32 v[16:17], v[4:5]
	v_mov_b64_e32 v[20:21], v[4:5]
	v_mov_b64_e32 v[24:25], v[4:5]
	v_mov_b64_e32 v[28:29], v[4:5]
	v_mov_b64_e32 v[32:33], v[4:5]
	v_mov_b32_e32 v42, v4
	v_mov_b32_e32 v43, v4
	v_mov_b32_e32 v44, v4
	v_mov_b32_e32 v45, v4
	s_branch .LBB1_135

	.amdhsa_kernel _Z13gather_kernelPK15HIP_vector_typeIjLj2EEPKiPK6OvfRecPKDF16_PKfPDF16_
		.amdhsa_group_segment_fixed_size 12112
		.amdhsa_private_segment_fixed_size 0
		.amdhsa_kernarg_size 48
		.amdhsa_user_sgpr_count 2
		.amdhsa_user_sgpr_dispatch_ptr 0
		.amdhsa_user_sgpr_queue_ptr 0
		.amdhsa_user_sgpr_kernarg_segment_ptr 1
		.amdhsa_user_sgpr_dispatch_id 0
		.amdhsa_user_sgpr_kernarg_preload_length 0
		.amdhsa_user_sgpr_kernarg_preload_offset 0
		.amdhsa_user_sgpr_private_segment_size 0
		.amdhsa_uses_dynamic_stack 0
		.amdhsa_enable_private_segment 0
		.amdhsa_system_sgpr_workgroup_id_x 1
		.amdhsa_system_sgpr_workgroup_id_y 0
		.amdhsa_system_sgpr_workgroup_id_z 0
		.amdhsa_system_sgpr_workgroup_info 0
		.amdhsa_system_vgpr_workitem_id 0
		.amdhsa_next_free_vgpr 72
		.amdhsa_next_free_sgpr 66
		.amdhsa_accum_offset 72
		.amdhsa_reserve_vcc 1
		.amdhsa_float_round_mode_32 0
		.amdhsa_float_round_mode_16_64 0
		.amdhsa_float_denorm_mode_32 3
		.amdhsa_float_denorm_mode_16_64 3
		.amdhsa_dx10_clamp 1
		.amdhsa_ieee_mode 1
		.amdhsa_fp16_overflow 0
		.amdhsa_tg_split 0
		.amdhsa_exception_fp_ieee_invalid_op 0
		.amdhsa_exception_fp_denorm_src 0
		.amdhsa_exception_fp_ieee_div_zero 0
		.amdhsa_exception_fp_ieee_overflow 0
		.amdhsa_exception_fp_ieee_underflow 0
		.amdhsa_exception_fp_ieee_inexact 0
		.amdhsa_exception_int_div_zero 0
	.end_amdhsa_kernel

amdhsa.kernels:
  - .agpr_count:     0
    .args:
      - .actual_access:  read_only
        .address_space:  global
        .offset:         0
        .size:           8
        .value_kind:     global_buffer
      - .actual_access:  read_only
        .address_space:  global
        .offset:         8
        .size:           8
        .value_kind:     global_buffer
      - .actual_access:  read_only
        .address_space:  global
        .offset:         16
        .size:           8
        .value_kind:     global_buffer
      - .actual_access:  read_only
        .address_space:  global
        .offset:         24
        .size:           8
        .value_kind:     global_buffer
      - .actual_access:  read_only
        .address_space:  global
        .offset:         32
        .size:           8
        .value_kind:     global_buffer
      - .address_space:  global
        .offset:         40
        .size:           8
        .value_kind:     global_buffer
      - .actual_access:  write_only
        .address_space:  global
        .offset:         48
        .size:           8
        .value_kind:     global_buffer
      - .actual_access:  write_only
        .address_space:  global
        .offset:         56
        .size:           8
        .value_kind:     global_buffer
      - .actual_access:  write_only
        .address_space:  global
        .offset:         64
        .size:           8
        .value_kind:     global_buffer
      - .actual_access:  write_only
        .address_space:  global
        .offset:         72
        .size:           8
        .value_kind:     global_buffer
      - .actual_access:  write_only
        .address_space:  global
        .offset:         80
        .size:           8
        .value_kind:     global_buffer
    .group_segment_fixed_size: 3132
    .kernarg_segment_align: 8
    .kernarg_segment_size: 88
    .language:       OpenCL C
    .language_version:
      - 2
      - 0
    .max_flat_workgroup_size: 256
    .name:           _Z11prep_kernelPKfPKiS0_S0_S0_PiP15HIP_vector_typeIjLj2EEP6OvfRecPDF16_S9_S9_
    .private_segment_fixed_size: 0
    .sgpr_count:     38
    .sgpr_spill_count: 0
    .symbol:         _Z11prep_kernelPKfPKiS0_S0_S0_PiP15HIP_vector_typeIjLj2EEP6OvfRecPDF16_S9_S9_.kd
    .uniform_work_group_size: 1
    .uses_dynamic_stack: false
    .vgpr_count:     42
    .vgpr_spill_count: 0
    .wavefront_size: 64
  - .agpr_count:     0
    .args:
      - .actual_access:  read_only
        .address_space:  global
        .offset:         0
        .size:           8
        .value_kind:     global_buffer
      - .actual_access:  read_only
        .address_space:  global
        .offset:         8
        .size:           8
        .value_kind:     global_buffer
      - .actual_access:  read_only
        .address_space:  global
        .offset:         16
        .size:           8
        .value_kind:     global_buffer
      - .address_space:  global
        .offset:         24
        .size:           8
        .value_kind:     global_buffer
      - .actual_access:  read_only
        .address_space:  global
        .offset:         32
        .size:           8
        .value_kind:     global_buffer
      - .actual_access:  write_only
        .address_space:  global
        .offset:         40
        .size:           8
        .value_kind:     global_buffer
    .group_segment_fixed_size: 12112
    .kernarg_segment_align: 8
    .kernarg_segment_size: 48
    .language:       OpenCL C
    .language_version:
      - 2
      - 0
    .max_flat_workgroup_size: 256
    .name:           _Z13gather_kernelPK15HIP_vector_typeIjLj2EEPKiPK6OvfRecPKDF16_PKfPDF16_
    .private_segment_fixed_size: 0
    .sgpr_count:     41
    .sgpr_spill_count: 0
    .symbol:         _Z13gather_kernelPK15HIP_vector_typeIjLj2EEPKiPK6OvfRecPKDF16_PKfPDF16_.kd
    .uniform_work_group_size: 1
    .uses_dynamic_stack: false
    .vgpr_count:     72
    .vgpr_spill_count: 0
    .wavefront_size: 64
  - .agpr_count:     0
    .args:
      - .actual_access:  read_only
        .address_space:  global
        .offset:         0
        .size:           8
        .value_kind:     global_buffer
      - .actual_access:  read_only
        .address_space:  global
        .offset:         8
        .size:           8
        .value_kind:     global_buffer
      - .actual_access:  read_only
        .address_space:  global
        .offset:         16
        .size:           8
        .value_kind:     global_buffer
      - .actual_access:  write_only
        .address_space:  global
        .offset:         24
        .size:           8
        .value_kind:     global_buffer
      - .actual_access:  read_only
        .address_space:  global
        .offset:         32
        .size:           8
        .value_kind:     global_buffer
      - .address_space:  global
        .offset:         40
        .size:           8
        .value_kind:     global_buffer
      - .actual_access:  read_only
        .address_space:  global
        .offset:         48
        .size:           8
        .value_kind:     global_buffer
      - .actual_access:  read_only
        .address_space:  global
        .offset:         56
        .size:           8
        .value_kind:     global_buffer
      - .actual_access:  read_only
        .address_space:  global
        .offset:         64
        .size:           8
        .value_kind:     global_buffer
      - .actual_access:  read_only
        .address_space:  global
        .offset:         72
        .size:           8
        .value_kind:     global_buffer
      - .offset:         80
        .size:           4
        .value_kind:     hidden_block_count_x
      - .offset:         84
        .size:           4
        .value_kind:     hidden_block_count_y
      - .offset:         88
        .size:           4
        .value_kind:     hidden_block_count_z
      - .offset:         92
        .size:           2
        .value_kind:     hidden_group_size_x
      - .offset:         94
        .size:           2
        .value_kind:     hidden_group_size_y
      - .offset:         96
        .size:           2
        .value_kind:     hidden_group_size_z
      - .offset:         98
        .size:           2
        .value_kind:     hidden_remainder_x
      - .offset:         100
        .size:           2
        .value_kind:     hidden_remainder_y
      - .offset:         102
        .size:           2
        .value_kind:     hidden_remainder_z
      - .offset:         120
        .size:           8
        .value_kind:     hidden_global_offset_x
      - .offset:         128
        .size:           8
        .value_kind:     hidden_global_offset_y
      - .offset:         136
        .size:           8
        .value_kind:     hidden_global_offset_z
      - .offset:         144
        .size:           2
        .value_kind:     hidden_grid_dims
    .group_segment_fixed_size: 33792
    .kernarg_segment_align: 8
    .kernarg_segment_size: 336
    .language:       OpenCL C
    .language_version:
      - 2
      - 0
    .max_flat_workgroup_size: 256
    .name:           _Z11gemm_kernelILi1EEvPKDF16_S1_PKfPDF16_PfS5_S3_S3_S1_S3_
    .private_segment_fixed_size: 0
    .sgpr_count:     27
    .sgpr_spill_count: 0
    .symbol:         _Z11gemm_kernelILi1EEvPKDF16_S1_PKfPDF16_PfS5_S3_S3_S1_S3_.kd
    .uniform_work_group_size: 1
    .uses_dynamic_stack: false
    .vgpr_count:     240
    .vgpr_spill_count: 0
    .wavefront_size: 64
  - .agpr_count:     0
    .args:
      - .actual_access:  read_only
        .address_space:  global
        .offset:         0
        .size:           8
        .value_kind:     global_buffer
      - .actual_access:  read_only
        .address_space:  global
        .offset:         8
        .size:           8
        .value_kind:     global_buffer
      - .actual_access:  read_only
        .address_space:  global
        .offset:         16
        .size:           8
        .value_kind:     global_buffer
      - .actual_access:  read_only
        .address_space:  global
        .offset:         24
        .size:           8
        .value_kind:     global_buffer
      - .actual_access:  write_only
        .address_space:  global
        .offset:         32
        .size:           8
        .value_kind:     global_buffer
      - .actual_access:  read_only
        .address_space:  global
        .offset:         40
        .size:           8
        .value_kind:     global_buffer
      - .actual_access:  read_only
        .address_space:  global
        .offset:         48
        .size:           8
        .value_kind:     global_buffer
      - .actual_access:  read_only
        .address_space:  global
        .offset:         56
        .size:           8
        .value_kind:     global_buffer
      - .actual_access:  read_only
        .address_space:  global
        .offset:         64
        .size:           8
        .value_kind:     global_buffer
      - .actual_access:  read_only
        .address_space:  global
        .offset:         72
        .size:           8
        .value_kind:     global_buffer
      - .offset:         80
        .size:           4
        .value_kind:     hidden_block_count_x
      - .offset:         84
        .size:           4
        .value_kind:     hidden_block_count_y
      - .offset:         88
        .size:           4
        .value_kind:     hidden_block_count_z
      - .offset:         92
        .size:           2
        .value_kind:     hidden_group_size_x
      - .offset:         94
        .size:           2
        .value_kind:     hidden_group_size_y
      - .offset:         96
        .size:           2
        .value_kind:     hidden_group_size_z
      - .offset:         98
        .size:           2
        .value_kind:     hidden_remainder_x
      - .offset:         100
        .size:           2
        .value_kind:     hidden_remainder_y
      - .offset:         102
        .size:           2
        .value_kind:     hidden_remainder_z
      - .offset:         120
        .size:           8
        .value_kind:     hidden_global_offset_x
      - .offset:         128
        .size:           8
        .value_kind:     hidden_global_offset_y
      - .offset:         136
        .size:           8
        .value_kind:     hidden_global_offset_z
      - .offset:         144
        .size:           2
        .value_kind:     hidden_grid_dims
    .group_segment_fixed_size: 33792
    .kernarg_segment_align: 8
    .kernarg_segment_size: 336
    .language:       OpenCL C
    .language_version:
      - 2
      - 0
    .max_flat_workgroup_size: 256
    .name:           _Z11gemm_kernelILi2EEvPKDF16_S1_PKfPDF16_PfS5_S3_S3_S1_S3_
    .private_segment_fixed_size: 0
    .sgpr_count:     23
    .sgpr_spill_count: 0
    .symbol:         _Z11gemm_kernelILi2EEvPKDF16_S1_PKfPDF16_PfS5_S3_S3_S1_S3_.kd
    .uniform_work_group_size: 1
    .uses_dynamic_stack: false
    .vgpr_count:     256
    .vgpr_spill_count: 0
    .wavefront_size: 64
